# plus MoE gate/up per-unit gather-offset loads batched (4 round trips to 1) and moe_build_table counter loads batched (8 to 1, 2 sites)
# baseline (speedup 1.0000x reference)
.LBB0_750:
	v_readlane_b32 s0, v253, 9
	v_readlane_b32 s8, v253, 7
	v_readlane_b32 s4, v253, 13
	v_readlane_b32 s5, v253, 14
	v_readlane_b32 s9, v253, 8
	s_waitcnt lgkmcnt(0)
	s_barrier
	v_readlane_b32 s1, v253, 10
	v_readlane_b32 s2, v253, 11
	v_readlane_b32 s3, v253, 12
	v_readlane_b32 s6, v253, 15
	v_readlane_b32 s7, v253, 16
	v_writelane_b32 v253, s8, 7
	s_add_u32 s20, s90, 1.0
	s_addc_u32 s21, s91, 0
	v_writelane_b32 v253, s9, 8
	v_writelane_b32 v253, s0, 9
	s_add_u32 s22, s90, 0x59800000
	s_addc_u32 s23, s91, 0
	v_writelane_b32 v253, s1, 10
	v_writelane_b32 v253, s2, 11
	v_writelane_b32 v253, s3, 12
	v_writelane_b32 v253, s4, 13
	v_writelane_b32 v253, s5, 14
	v_writelane_b32 v253, s6, 15
	s_add_u32 s24, s90, 0x280000
	v_writelane_b32 v253, s7, 16
	s_addc_u32 s25, s91, 0
	s_lshl_b32 s1, s58, 5
	s_ashr_i32 s70, s76, 31
	s_and_b32 s19, s1, 0x60
	s_lshr_b32 s1, s70, 29
	s_add_i32 s1, s76, s1
	s_ashr_i32 s0, s58, 2
	s_ashr_i32 s48, s1, 3
	s_and_b32 s1, s1, -8
	s_lshl_b32 s59, s58, 10
	s_lshl_b32 s62, s0, 6
	s_lshl_b32 s61, s0, 13
	s_lshr_b32 s49, s19, 3
	s_sub_i32 s52, s76, s1
	s_cmp_lt_i32 s52, 0
	s_cselect_b64 s[56:57], -1, 0
	s_cmp_eq_u32 s0, 1
	v_readlane_b32 s2, v254, 50
	s_cselect_b64 s[28:29], -1, 0
	s_cmp_lt_u32 s58, 4
	v_readlane_b32 s3, v254, 51
	s_cselect_b64 s[36:37], -1, 0
	s_ashr_i32 s75, s83, 31
	s_mov_b64 s[0:1], -1
	s_and_b64 vcc, exec, s[2:3]
	v_mbcnt_lo_u32_b32 v1, -1, 0
	v_mbcnt_hi_u32_b32 v1, -1, v1
	s_cbranch_vccz .LBB0_773
	v_lshl_add_u32 v0, s58, 6, v1
	v_readlane_b32 s2, v253, 7
	v_readlane_b32 s3, v253, 8
	s_nop 4
	global_load_dword v2, v97, s[2:3] offset:1024 sc1
	global_load_dword v3, v97, s[2:3] offset:1280 sc1
	global_load_dword v4, v97, s[2:3] offset:1536 sc1
	global_load_dword v5, v97, s[2:3] offset:1792 sc1
	global_load_dword v6, v97, s[2:3] offset:2048 sc1
	global_load_dword v7, v97, s[2:3] offset:2304 sc1
	global_load_dword v8, v97, s[2:3] offset:2560 sc1
	global_load_dword v9, v97, s[2:3] offset:2816 sc1
	s_waitcnt vmcnt(0)
	v_readfirstlane_b32 s4, v2
	v_readfirstlane_b32 s6, v3
	v_readfirstlane_b32 s8, v4
	v_readfirstlane_b32 s10, v5
	v_readfirstlane_b32 s12, v6
	v_readfirstlane_b32 s14, v7
	v_readfirstlane_b32 s16, v8
	v_readfirstlane_b32 s18, v9
	s_add_i32 s0, s4, 0xff
	s_ashr_i32 s5, s0, 8
	s_add_i32 s0, s6, 0xff
	s_ashr_i32 s7, s0, 8
	s_add_i32 s7, s7, s5
	s_add_i32 s0, s8, 0xff
	s_ashr_i32 s9, s0, 8
	s_add_i32 s9, s9, s7
	s_add_i32 s0, s10, 0xff
	s_ashr_i32 s11, s0, 8
	s_add_i32 s11, s11, s9
	s_add_i32 s0, s12, 0xff
	s_ashr_i32 s13, s0, 8
	s_add_i32 s13, s13, s11
	s_add_i32 s0, s14, 0xff
	s_ashr_i32 s15, s0, 8
	s_add_i32 s15, s15, s13
	s_add_i32 s0, s16, 0xff
	s_ashr_i32 s17, s0, 8
	s_add_i32 s17, s17, s15
	s_barrier
	s_add_i32 s0, s18, 0xff
	s_ashr_i32 s53, s0, 8
	s_add_i32 s53, s53, s17
	v_cmp_gt_i32_e32 vcc, s53, v0
	s_and_saveexec_b64 s[0:1], vcc
	s_cbranch_execz .LBB0_754
	s_add_i32 s2, 0, 0x20000
	v_lshlrev_b32_e32 v2, 8, v0
	v_lshl_add_u32 v1, v0, 4, s2
	v_sub_u32_e32 v3, 0, v2
	s_mov_b64 s[2:3], 0

.LBB0_762:
	s_nop 0
	v_cndmask_b32_e64 v0, 0, 1, s[6:7]
	v_cmp_ne_u32_e64 s[4:5], 1, v0
	s_andn2_b64 vcc, exec, s[6:7]
	v_mov_b32_e32 v219, v166
	v_mov_b32_e32 v221, v178
	v_mov_b32_e32 v220, v168
	v_mov_b32_e32 v222, v180
	s_cbranch_vccnz .LBB0_764
	v_cmp_gt_i32_e32 vcc, s64, v194
	s_nop 1
	v_cndmask_b32_e32 v0, 0, v194, vcc
	v_cmp_gt_i32_e32 vcc, s64, v200
	s_nop 1
	v_cndmask_b32_e32 v2, 0, v200, vcc
	v_cmp_gt_i32_e32 vcc, s64, v196
	s_nop 1
	v_cndmask_b32_e32 v4, 0, v196, vcc
	v_cmp_gt_i32_e32 vcc, s64, v201
	s_nop 1
	v_cndmask_b32_e32 v6, 0, v201, vcc
	v_ashrrev_i32_e32 v1, 31, v0
	v_ashrrev_i32_e32 v3, 31, v2
	v_ashrrev_i32_e32 v5, 31, v4
	v_ashrrev_i32_e32 v7, 31, v6
	v_lshl_add_u64 v[0:1], v[0:1], 3, s[62:63]
	v_lshl_add_u64 v[2:3], v[2:3], 3, s[62:63]
	v_lshl_add_u64 v[4:5], v[4:5], 3, s[62:63]
	v_lshl_add_u64 v[6:7], v[6:7], 3, s[62:63]
	global_load_dword v0, v[0:1], off
	global_load_dword v2, v[2:3], off
	global_load_dword v4, v[4:5], off
	global_load_dword v6, v[6:7], off
	s_waitcnt vmcnt(0)
	v_lshl_add_u32 v219, v0, 12, v195
	v_lshl_add_u32 v220, v2, 12, v195
	v_lshl_add_u32 v221, v4, 12, v197
	v_lshl_add_u32 v222, v6, 12, v197

.LBB0_844:
	v_readlane_b32 s0, v253, 9
	v_readlane_b32 s8, v253, 7
	v_readlane_b32 s4, v253, 13
	v_readlane_b32 s5, v253, 14
	v_readlane_b32 s9, v253, 8
	s_waitcnt lgkmcnt(0)
	s_barrier
	v_readlane_b32 s1, v253, 10
	v_readlane_b32 s2, v253, 11
	v_readlane_b32 s3, v253, 12
	v_readlane_b32 s6, v253, 15
	v_readlane_b32 s7, v253, 16
	v_writelane_b32 v253, s8, 7
	s_add_u32 s36, s90, 0x59800000
	s_addc_u32 s37, s91, 0
	v_writelane_b32 v253, s9, 8
	v_writelane_b32 v253, s0, 9
	s_ashr_i32 s49, s76, 31
	s_lshl_b32 s48, s58, 10
	v_writelane_b32 v253, s1, 10
	v_writelane_b32 v253, s2, 11
	v_writelane_b32 v253, s3, 12
	v_writelane_b32 v253, s4, 13
	v_writelane_b32 v253, s5, 14
	v_writelane_b32 v253, s6, 15
	v_writelane_b32 v253, s7, 16
	s_lshl_b32 s1, s58, 5
	s_and_b32 s53, s1, 0x60
	s_lshr_b32 s1, s49, 29
	s_add_i32 s1, s76, s1
	s_ashr_i32 s0, s58, 2
	s_ashr_i32 s62, s1, 3
	s_and_b32 s1, s1, -8
	s_lshl_b32 s56, s0, 6
	s_lshl_b32 s29, s0, 13
	s_lshr_b32 s88, s53, 3
	s_sub_i32 s63, s76, s1
	s_cmp_lt_i32 s63, 0
	s_cselect_b64 s[78:79], -1, 0
	s_cmp_eq_u32 s0, 1
	v_readlane_b32 s4, v254, 50
	s_cselect_b64 s[0:1], -1, 0
	s_cmp_lt_u32 s58, 4
	v_readlane_b32 s5, v254, 51
	s_cselect_b64 s[6:7], -1, 0
	s_ashr_i32 s52, s83, 31
	s_mov_b64 s[2:3], -1
	s_and_b64 vcc, exec, s[4:5]
	v_mbcnt_lo_u32_b32 v1, -1, 0
	v_mbcnt_hi_u32_b32 v1, -1, v1
	s_cbranch_vccz .LBB0_865
	v_lshl_add_u32 v0, s58, 6, v1
	v_readlane_b32 s4, v253, 7
	v_readlane_b32 s5, v253, 8
	s_nop 4
	global_load_dword v2, v97, s[4:5] offset:1024 sc1
	global_load_dword v3, v97, s[4:5] offset:1280 sc1
	global_load_dword v4, v97, s[4:5] offset:1536 sc1
	global_load_dword v5, v97, s[4:5] offset:1792 sc1
	global_load_dword v6, v97, s[4:5] offset:2048 sc1
	global_load_dword v7, v97, s[4:5] offset:2304 sc1
	global_load_dword v8, v97, s[4:5] offset:2560 sc1
	global_load_dword v9, v97, s[4:5] offset:2816 sc1
	s_waitcnt vmcnt(0)
	v_readfirstlane_b32 s10, v2
	v_readfirstlane_b32 s12, v3
	v_readfirstlane_b32 s14, v4
	v_readfirstlane_b32 s16, v5
	v_readfirstlane_b32 s18, v6
	v_readfirstlane_b32 s20, v7
	v_readfirstlane_b32 s22, v8
	v_readfirstlane_b32 s24, v9
	s_add_i32 s2, s10, 0xff
	s_ashr_i32 s11, s2, 8
	s_add_i32 s2, s12, 0xff
	s_ashr_i32 s13, s2, 8
	s_add_i32 s13, s13, s11
	s_add_i32 s2, s14, 0xff
	s_ashr_i32 s15, s2, 8
	s_add_i32 s15, s15, s13
	s_add_i32 s2, s16, 0xff
	s_ashr_i32 s17, s2, 8
	s_add_i32 s17, s17, s15
	s_add_i32 s2, s18, 0xff
	s_ashr_i32 s19, s2, 8
	s_add_i32 s19, s19, s17
	s_add_i32 s2, s20, 0xff
	s_ashr_i32 s21, s2, 8
	s_add_i32 s21, s21, s19
	s_add_i32 s2, s22, 0xff
	s_ashr_i32 s23, s2, 8
	s_add_i32 s23, s23, s21
	s_barrier
	s_add_i32 s2, s24, 0xff
	s_ashr_i32 s64, s2, 8
	s_add_i32 s64, s64, s23
	v_cmp_gt_i32_e32 vcc, s64, v0
	s_and_saveexec_b64 s[2:3], vcc
	s_cbranch_execz .LBB0_848
	s_add_i32 s4, 0, 0x20000
	v_lshlrev_b32_e32 v2, 8, v0
	v_lshl_add_u32 v1, v0, 4, s4
	v_sub_u32_e32 v3, 0, v2
	s_mov_b64 s[4:5], 0
